# v74 + differential-attention epilogue: the 16 sub-layer-norm gain loads issued together with counted waits instead of one blocking round trip each
# speedup vs baseline: 1.0124x; 1.0124x over previous
.LBB0_3653:
	s_cmp_gt_u32 s79, 3
	v_readlane_b32 s43, v254, 8
	s_mov_b64 s[50:51], s[80:81]
	s_waitcnt lgkmcnt(0)
	s_barrier
	s_cbranch_scc1 .LBB0_3655
	v_readlane_b32 s4, v255, 36
	v_readlane_b32 s5, v255, 37
	s_add_u32 s4, s38, s4
	s_addc_u32 s5, s39, s5
	v_lshlrev_b32_e32 v3, 2, v129
	ds_read2st64_b32 v[136:137], v0 offset1:1
	ds_read2st64_b32 v[14:15], v0 offset0:2 offset1:3
	ds_read2st64_b32 v[12:13], v0 offset0:4 offset1:5
	ds_read2st64_b32 v[10:11], v0 offset0:6 offset1:7
	ds_read2st64_b32 v[126:127], v0 offset0:8 offset1:9
	ds_read2st64_b32 v[130:131], v0 offset0:10 offset1:11
	ds_read2st64_b32 v[132:133], v0 offset0:12 offset1:13
	ds_read2st64_b32 v[134:135], v0 offset0:14 offset1:15
	ds_read2st64_b32 v[118:119], v0 offset0:16 offset1:17
	ds_read2st64_b32 v[120:121], v0 offset0:18 offset1:19
	ds_read2st64_b32 v[122:123], v0 offset0:20 offset1:21
	ds_read2st64_b32 v[124:125], v0 offset0:22 offset1:23
	ds_read2st64_b32 v[110:111], v0 offset0:24 offset1:25
	ds_read2st64_b32 v[112:113], v0 offset0:26 offset1:27
	ds_read2st64_b32 v[114:115], v0 offset0:28 offset1:29
	ds_read2st64_b32 v[116:117], v0 offset0:30 offset1:31
	ds_read2st64_b32 v[102:103], v0 offset0:32 offset1:33
	ds_read2st64_b32 v[104:105], v0 offset0:34 offset1:35
	ds_read2st64_b32 v[106:107], v0 offset0:36 offset1:37
	ds_read2st64_b32 v[108:109], v0 offset0:38 offset1:39
	ds_read2st64_b32 v[94:95], v0 offset0:40 offset1:41
	ds_read2st64_b32 v[96:97], v0 offset0:42 offset1:43
	ds_read2st64_b32 v[98:99], v0 offset0:44 offset1:45
	ds_read2st64_b32 v[100:101], v0 offset0:46 offset1:47
	ds_read2st64_b32 v[86:87], v0 offset0:48 offset1:49
	ds_read2st64_b32 v[88:89], v0 offset0:50 offset1:51
	ds_read2st64_b32 v[90:91], v0 offset0:52 offset1:53
	ds_read2st64_b32 v[92:93], v0 offset0:54 offset1:55
	ds_read2st64_b32 v[6:7], v0 offset0:56 offset1:57
	ds_read2st64_b32 v[80:81], v0 offset0:58 offset1:59
	ds_read2st64_b32 v[82:83], v0 offset0:60 offset1:61
	ds_read2st64_b32 v[84:85], v0 offset0:62 offset1:63
	global_load_dwordx4 v[156:159], v3, s[4:5] offset:32
	global_load_dwordx4 v[160:163], v3, s[4:5]
	global_load_dwordx4 v[164:167], v3, s[4:5] offset:96
	global_load_dwordx4 v[168:171], v3, s[4:5] offset:64
	global_load_dwordx4 v[172:175], v3, s[4:5] offset:160
	global_load_dwordx4 v[176:179], v3, s[4:5] offset:128
	global_load_dwordx4 v[180:183], v3, s[4:5] offset:224
	global_load_dwordx4 v[186:189], v3, s[4:5] offset:192
	global_load_dwordx4 v[198:201], v3, s[4:5] offset:288
	global_load_dwordx4 v[202:205], v3, s[4:5] offset:256
	global_load_dwordx4 v[206:209], v3, s[4:5] offset:352
	global_load_dwordx4 v[210:213], v3, s[4:5] offset:320
	global_load_dwordx4 v[214:217], v3, s[4:5] offset:416
	global_load_dwordx4 v[242:245], v3, s[4:5] offset:384
	global_load_dwordx4 v[246:249], v3, s[4:5] offset:480
	global_load_dwordx4 v[250:253], v3, s[4:5] offset:448
	s_waitcnt lgkmcnt(14)
	v_pk_mul_f32 v[12:13], v[148:149], v[12:13]
	v_lshlrev_b32_e32 v0, 12, v128
	v_pk_fma_f32 v[128:129], v[68:69], v[2:3], v[12:13] op_sel_hi:[1,0,1] neg_lo:[0,0,1] neg_hi:[0,0,1]
	v_pk_mul_f32 v[14:15], v[148:149], v[14:15]
	v_lshl_add_u64 v[4:5], s[84:85], 0, v[0:1]
	s_lshl_b32 s92, s2, 1
	v_cmp_gt_u32_e32 vcc, 32, v153
	v_lshl_add_u64 v[4:5], v[4:5], 0, s[92:93]
	v_pk_mul_f32 v[10:11], v[148:149], v[10:11]
	v_cndmask_b32_e64 v0, 16, 0, vcc
	v_lshl_add_u64 v[8:9], v[4:5], 0, v[0:1]
	v_pk_fma_f32 v[70:71], v[70:71], v[2:3], v[10:11] op_sel_hi:[1,0,1] neg_lo:[0,0,1] neg_hi:[0,0,1]
	s_waitcnt lgkmcnt(11)
	v_pk_mul_f32 v[94:95], v[148:149], v[94:95]
	s_waitcnt lgkmcnt(10)
	v_pk_mul_f32 v[96:97], v[148:149], v[96:97]
	v_pk_fma_f32 v[94:95], v[40:41], v[2:3], v[94:95] op_sel_hi:[1,0,1] neg_lo:[0,0,1] neg_hi:[0,0,1]
	s_waitcnt lgkmcnt(2)
	v_pk_mul_f32 v[80:81], v[148:149], v[80:81]
	v_pk_mul_f32 v[6:7], v[148:149], v[6:7]
	v_pk_fma_f32 v[80:81], v[26:27], v[2:3], v[80:81] op_sel_hi:[1,0,1] neg_lo:[0,0,1] neg_hi:[0,0,1]
	s_mov_b64 s[2:3], 0x38400c00
	v_lshl_add_u64 v[4:5], v[8:9], 0, s[2:3]
	s_waitcnt vmcnt(15)
	v_pk_mul_f32 v[12:13], v[128:129], v[156:157]
	v_pk_fma_f32 v[138:139], v[66:67], v[2:3], v[14:15] op_sel_hi:[1,0,1] neg_lo:[0,0,1] neg_hi:[0,0,1]
	v_pk_mul_f32 v[10:11], v[70:71], v[158:159]
	s_waitcnt vmcnt(14)
	v_pk_mul_f32 v[14:15], v[138:139], v[162:163]
	v_pk_mul_f32 v[68:69], v[148:149], v[136:137]
	s_nop 0
	v_pk_fma_f32 v[64:65], v[64:65], v[2:3], v[68:69] op_sel_hi:[1,0,1] neg_lo:[0,0,1] neg_hi:[0,0,1]
	s_nop 0
	v_mul_f32_e32 v0, v65, v65
	v_pk_fma_f32 v[68:69], v[64:65], v[64:65], v[0:1] op_sel_hi:[1,1,0]
	v_pk_mul_f32 v[64:65], v[64:65], v[160:161]
	v_pk_fma_f32 v[66:67], v[138:139], v[138:139], v[68:69]
	v_mul_f32_e32 v0, v139, v139
	v_pk_add_f32 v[66:67], v[66:67], v[0:1] op_sel_hi:[1,0]
	v_mul_f32_e32 v0, v129, v129
	v_pk_fma_f32 v[66:67], v[128:129], v[128:129], v[66:67]
	s_nop 0
	v_pk_add_f32 v[66:67], v[66:67], v[0:1] op_sel_hi:[1,0]
	v_mul_f32_e32 v0, v71, v71
	v_pk_fma_f32 v[66:67], v[70:71], v[70:71], v[66:67]
	v_pk_add_f32 v[128:129], v[66:67], v[0:1] op_sel_hi:[1,0]
	v_pk_mul_f32 v[66:67], v[148:149], v[134:135]
	s_nop 0
	v_pk_fma_f32 v[78:79], v[78:79], v[2:3], v[66:67] op_sel_hi:[1,0,1] neg_lo:[0,0,1] neg_hi:[0,0,1]
	s_waitcnt vmcnt(13)
	v_pk_mul_f32 v[66:67], v[78:79], v[166:167]
	v_pk_mul_f32 v[70:71], v[148:149], v[132:133]
	s_nop 0
	v_pk_fma_f32 v[132:133], v[76:77], v[2:3], v[70:71] op_sel_hi:[1,0,1] neg_lo:[0,0,1] neg_hi:[0,0,1]
	v_pk_mul_f32 v[70:71], v[148:149], v[130:131]
	v_pk_mul_f32 v[68:69], v[132:133], v[164:165]
	v_pk_fma_f32 v[130:131], v[74:75], v[2:3], v[70:71] op_sel_hi:[1,0,1] neg_lo:[0,0,1] neg_hi:[0,0,1]
	s_waitcnt vmcnt(12)
	v_pk_mul_f32 v[70:71], v[130:131], v[170:171]
	v_pk_mul_f32 v[76:77], v[148:149], v[126:127]
	s_nop 0
	v_pk_fma_f32 v[76:77], v[72:73], v[2:3], v[76:77] op_sel_hi:[1,0,1] neg_lo:[0,0,1] neg_hi:[0,0,1]
	s_nop 0
	v_pk_mul_f32 v[72:73], v[76:77], v[168:169]
	v_pk_fma_f32 v[74:75], v[76:77], v[76:77], v[128:129]
	v_mul_f32_e32 v0, v77, v77
	v_pk_add_f32 v[74:75], v[74:75], v[0:1] op_sel_hi:[1,0]
	v_mul_f32_e32 v0, v131, v131
	v_pk_fma_f32 v[74:75], v[130:131], v[130:131], v[74:75]
	s_nop 0
	v_pk_add_f32 v[74:75], v[74:75], v[0:1] op_sel_hi:[1,0]
	v_mul_f32_e32 v0, v133, v133
	v_pk_fma_f32 v[74:75], v[132:133], v[132:133], v[74:75]
	s_nop 0
	v_pk_add_f32 v[74:75], v[74:75], v[0:1] op_sel_hi:[1,0]
	v_mul_f32_e32 v0, v79, v79
	v_pk_fma_f32 v[74:75], v[78:79], v[78:79], v[74:75]
	s_nop 0
	v_pk_add_f32 v[78:79], v[74:75], v[0:1] op_sel_hi:[1,0]
	v_pk_mul_f32 v[74:75], v[148:149], v[124:125]
	s_nop 0
	v_pk_fma_f32 v[124:125], v[54:55], v[2:3], v[74:75] op_sel_hi:[1,0,1] neg_lo:[0,0,1] neg_hi:[0,0,1]
	s_waitcnt vmcnt(11)
	v_pk_mul_f32 v[54:55], v[124:125], v[174:175]
	v_pk_mul_f32 v[76:77], v[148:149], v[122:123]
	s_nop 0
	v_pk_fma_f32 v[122:123], v[52:53], v[2:3], v[76:77] op_sel_hi:[1,0,1] neg_lo:[0,0,1] neg_hi:[0,0,1]
	s_nop 0
	v_pk_mul_f32 v[52:53], v[122:123], v[172:173]
	v_pk_mul_f32 v[74:75], v[148:149], v[120:121]
	s_nop 0
	v_pk_fma_f32 v[120:121], v[50:51], v[2:3], v[74:75] op_sel_hi:[1,0,1] neg_lo:[0,0,1] neg_hi:[0,0,1]
	s_waitcnt vmcnt(10)
	v_pk_mul_f32 v[50:51], v[120:121], v[178:179]
	v_pk_mul_f32 v[76:77], v[148:149], v[118:119]
	s_nop 0
	v_pk_fma_f32 v[76:77], v[48:49], v[2:3], v[76:77] op_sel_hi:[1,0,1] neg_lo:[0,0,1] neg_hi:[0,0,1]
	s_nop 0
	v_pk_mul_f32 v[48:49], v[76:77], v[176:177]
	v_pk_fma_f32 v[74:75], v[76:77], v[76:77], v[78:79]
	v_mul_f32_e32 v0, v77, v77
	v_pk_add_f32 v[74:75], v[74:75], v[0:1] op_sel_hi:[1,0]
	v_mul_f32_e32 v0, v121, v121
	v_pk_fma_f32 v[74:75], v[120:121], v[120:121], v[74:75]
	s_nop 0
	v_pk_add_f32 v[74:75], v[74:75], v[0:1] op_sel_hi:[1,0]
	v_mul_f32_e32 v0, v123, v123
	v_pk_fma_f32 v[74:75], v[122:123], v[122:123], v[74:75]
	s_nop 0
	v_pk_add_f32 v[74:75], v[74:75], v[0:1] op_sel_hi:[1,0]
	v_mul_f32_e32 v0, v125, v125
	v_pk_fma_f32 v[74:75], v[124:125], v[124:125], v[74:75]
	s_nop 0
	v_pk_add_f32 v[78:79], v[74:75], v[0:1] op_sel_hi:[1,0]
	v_pk_mul_f32 v[74:75], v[148:149], v[116:117]
	s_nop 0
	v_pk_fma_f32 v[116:117], v[62:63], v[2:3], v[74:75] op_sel_hi:[1,0,1] neg_lo:[0,0,1] neg_hi:[0,0,1]
	s_waitcnt vmcnt(9)
	v_pk_mul_f32 v[62:63], v[116:117], v[182:183]
	v_pk_mul_f32 v[76:77], v[148:149], v[114:115]
	s_nop 0
	v_pk_fma_f32 v[114:115], v[60:61], v[2:3], v[76:77] op_sel_hi:[1,0,1] neg_lo:[0,0,1] neg_hi:[0,0,1]
	s_nop 0
	v_pk_mul_f32 v[60:61], v[114:115], v[180:181]
	v_pk_mul_f32 v[74:75], v[148:149], v[112:113]
	s_nop 0
	v_pk_fma_f32 v[112:113], v[58:59], v[2:3], v[74:75] op_sel_hi:[1,0,1] neg_lo:[0,0,1] neg_hi:[0,0,1]
	s_waitcnt vmcnt(8)
	v_pk_mul_f32 v[58:59], v[112:113], v[188:189]
	v_pk_mul_f32 v[76:77], v[148:149], v[110:111]
	s_nop 0
	v_pk_fma_f32 v[76:77], v[56:57], v[2:3], v[76:77] op_sel_hi:[1,0,1] neg_lo:[0,0,1] neg_hi:[0,0,1]
	s_nop 0
	v_pk_mul_f32 v[56:57], v[76:77], v[186:187]
	v_pk_fma_f32 v[74:75], v[76:77], v[76:77], v[78:79]
	v_mul_f32_e32 v0, v77, v77
	v_pk_add_f32 v[74:75], v[74:75], v[0:1] op_sel_hi:[1,0]
	v_mul_f32_e32 v0, v113, v113
	v_pk_fma_f32 v[74:75], v[112:113], v[112:113], v[74:75]
	s_nop 0
	v_pk_add_f32 v[74:75], v[74:75], v[0:1] op_sel_hi:[1,0]
	v_mul_f32_e32 v0, v115, v115
	v_pk_fma_f32 v[74:75], v[114:115], v[114:115], v[74:75]
	s_nop 0
	v_pk_add_f32 v[74:75], v[74:75], v[0:1] op_sel_hi:[1,0]
	v_mul_f32_e32 v0, v117, v117
	v_pk_fma_f32 v[74:75], v[116:117], v[116:117], v[74:75]
	s_nop 0
	v_pk_add_f32 v[78:79], v[74:75], v[0:1] op_sel_hi:[1,0]
	v_pk_mul_f32 v[74:75], v[148:149], v[108:109]
	s_nop 0
	v_pk_fma_f32 v[108:109], v[38:39], v[2:3], v[74:75] op_sel_hi:[1,0,1] neg_lo:[0,0,1] neg_hi:[0,0,1]
	s_waitcnt vmcnt(7)
	v_pk_mul_f32 v[38:39], v[108:109], v[200:201]
	v_pk_mul_f32 v[76:77], v[148:149], v[106:107]
	s_nop 0
	v_pk_fma_f32 v[106:107], v[36:37], v[2:3], v[76:77] op_sel_hi:[1,0,1] neg_lo:[0,0,1] neg_hi:[0,0,1]
	s_nop 0
	v_pk_mul_f32 v[36:37], v[106:107], v[198:199]
	v_pk_mul_f32 v[74:75], v[148:149], v[104:105]
	s_nop 0
	v_pk_fma_f32 v[104:105], v[34:35], v[2:3], v[74:75] op_sel_hi:[1,0,1] neg_lo:[0,0,1] neg_hi:[0,0,1]
	s_waitcnt vmcnt(6)
	v_pk_mul_f32 v[34:35], v[104:105], v[204:205]
	v_pk_mul_f32 v[76:77], v[148:149], v[102:103]
	s_nop 0
	v_pk_fma_f32 v[76:77], v[32:33], v[2:3], v[76:77] op_sel_hi:[1,0,1] neg_lo:[0,0,1] neg_hi:[0,0,1]
	s_nop 0
	v_pk_mul_f32 v[32:33], v[76:77], v[202:203]
	v_pk_fma_f32 v[74:75], v[76:77], v[76:77], v[78:79]
	v_mul_f32_e32 v0, v77, v77
	v_pk_add_f32 v[74:75], v[74:75], v[0:1] op_sel_hi:[1,0]
	v_mul_f32_e32 v0, v105, v105
	v_pk_fma_f32 v[74:75], v[104:105], v[104:105], v[74:75]
	v_pk_mul_f32 v[78:79], v[148:149], v[98:99]
	v_pk_add_f32 v[74:75], v[74:75], v[0:1] op_sel_hi:[1,0]
	v_mul_f32_e32 v0, v107, v107
	v_pk_fma_f32 v[74:75], v[106:107], v[106:107], v[74:75]
	v_pk_fma_f32 v[78:79], v[44:45], v[2:3], v[78:79] op_sel_hi:[1,0,1] neg_lo:[0,0,1] neg_hi:[0,0,1]
	v_pk_add_f32 v[74:75], v[74:75], v[0:1] op_sel_hi:[1,0]
	v_mul_f32_e32 v0, v109, v109
	v_pk_fma_f32 v[74:75], v[108:109], v[108:109], v[74:75]
	s_nop 0
	v_pk_add_f32 v[76:77], v[74:75], v[0:1] op_sel_hi:[1,0]
	v_pk_mul_f32 v[74:75], v[148:149], v[100:101]
	v_pk_fma_f32 v[76:77], v[94:95], v[94:95], v[76:77]
	v_mul_f32_e32 v0, v95, v95
	v_pk_add_f32 v[76:77], v[76:77], v[0:1] op_sel_hi:[1,0]
	v_pk_fma_f32 v[74:75], v[46:47], v[2:3], v[74:75] op_sel_hi:[1,0,1] neg_lo:[0,0,1] neg_hi:[0,0,1]
	s_waitcnt vmcnt(5)
	v_pk_mul_f32 v[44:45], v[78:79], v[206:207]
	v_pk_fma_f32 v[100:101], v[42:43], v[2:3], v[96:97] op_sel_hi:[1,0,1] neg_lo:[0,0,1] neg_hi:[0,0,1]
	v_pk_mul_f32 v[46:47], v[74:75], v[208:209]
	v_pk_fma_f32 v[76:77], v[100:101], v[100:101], v[76:77]
	v_mul_f32_e32 v0, v101, v101
	v_pk_add_f32 v[76:77], v[76:77], v[0:1] op_sel_hi:[1,0]
	v_mul_f32_e32 v0, v79, v79
	v_pk_fma_f32 v[76:77], v[78:79], v[78:79], v[76:77]
	v_pk_add_f32 v[76:77], v[76:77], v[0:1] op_sel_hi:[1,0]
	v_mul_f32_e32 v0, v75, v75
	v_pk_fma_f32 v[76:77], v[74:75], v[74:75], v[76:77]
	v_pk_mul_f32 v[74:75], v[148:149], v[92:93]
	v_pk_add_f32 v[78:79], v[76:77], v[0:1] op_sel_hi:[1,0]
	v_pk_fma_f32 v[92:93], v[22:23], v[2:3], v[74:75] op_sel_hi:[1,0,1] neg_lo:[0,0,1] neg_hi:[0,0,1]
	s_waitcnt vmcnt(4)
	v_pk_mul_f32 v[40:41], v[94:95], v[210:211]
	v_pk_mul_f32 v[42:43], v[100:101], v[212:213]
	s_waitcnt vmcnt(3)
	v_pk_mul_f32 v[22:23], v[92:93], v[216:217]
	v_pk_mul_f32 v[76:77], v[148:149], v[90:91]
	s_nop 0
	v_pk_fma_f32 v[90:91], v[20:21], v[2:3], v[76:77] op_sel_hi:[1,0,1] neg_lo:[0,0,1] neg_hi:[0,0,1]
	s_nop 0
	v_pk_mul_f32 v[20:21], v[90:91], v[214:215]
	v_pk_mul_f32 v[74:75], v[148:149], v[88:89]
	s_nop 0
	v_pk_fma_f32 v[88:89], v[18:19], v[2:3], v[74:75] op_sel_hi:[1,0,1] neg_lo:[0,0,1] neg_hi:[0,0,1]
	s_waitcnt vmcnt(2)
	v_pk_mul_f32 v[18:19], v[88:89], v[244:245]
	v_pk_mul_f32 v[76:77], v[148:149], v[86:87]
	s_nop 0
	v_pk_fma_f32 v[76:77], v[16:17], v[2:3], v[76:77] op_sel_hi:[1,0,1] neg_lo:[0,0,1] neg_hi:[0,0,1]
	s_nop 0
	v_pk_mul_f32 v[16:17], v[76:77], v[242:243]
	v_pk_fma_f32 v[74:75], v[76:77], v[76:77], v[78:79]
	v_mul_f32_e32 v0, v77, v77
	v_pk_add_f32 v[74:75], v[74:75], v[0:1] op_sel_hi:[1,0]
	v_mul_f32_e32 v0, v89, v89
	v_pk_fma_f32 v[74:75], v[88:89], v[88:89], v[74:75]
	s_waitcnt lgkmcnt(1)
	v_pk_mul_f32 v[78:79], v[148:149], v[82:83]
	v_pk_add_f32 v[74:75], v[74:75], v[0:1] op_sel_hi:[1,0]
	v_mul_f32_e32 v0, v91, v91
	v_pk_fma_f32 v[74:75], v[90:91], v[90:91], v[74:75]
	v_pk_fma_f32 v[78:79], v[28:29], v[2:3], v[78:79] op_sel_hi:[1,0,1] neg_lo:[0,0,1] neg_hi:[0,0,1]
	v_pk_add_f32 v[74:75], v[74:75], v[0:1] op_sel_hi:[1,0]
	v_mul_f32_e32 v0, v93, v93
	v_pk_fma_f32 v[74:75], v[92:93], v[92:93], v[74:75]
	s_nop 0
	v_pk_add_f32 v[76:77], v[74:75], v[0:1] op_sel_hi:[1,0]
	s_waitcnt lgkmcnt(0)
	v_pk_mul_f32 v[74:75], v[148:149], v[84:85]
	v_pk_fma_f32 v[74:75], v[30:31], v[2:3], v[74:75] op_sel_hi:[1,0,1] neg_lo:[0,0,1] neg_hi:[0,0,1]
	s_waitcnt vmcnt(1)
	v_pk_mul_f32 v[28:29], v[78:79], v[246:247]
	v_pk_fma_f32 v[2:3], v[24:25], v[2:3], v[6:7] op_sel_hi:[1,0,1] neg_lo:[0,0,1] neg_hi:[0,0,1]
	v_pk_mul_f32 v[30:31], v[74:75], v[248:249]
	v_pk_fma_f32 v[6:7], v[2:3], v[2:3], v[76:77]
	v_mul_f32_e32 v0, v3, v3
	s_waitcnt vmcnt(0)
	v_pk_mul_f32 v[24:25], v[2:3], v[250:251]
	v_pk_add_f32 v[2:3], v[6:7], v[0:1] op_sel_hi:[1,0]
	v_mul_f32_e32 v0, v81, v81
	v_pk_fma_f32 v[2:3], v[80:81], v[80:81], v[2:3]
	v_pk_mul_f32 v[26:27], v[80:81], v[252:253]
	v_pk_add_f32 v[2:3], v[2:3], v[0:1] op_sel_hi:[1,0]
	v_mul_f32_e32 v0, v79, v79
	v_pk_fma_f32 v[2:3], v[78:79], v[78:79], v[2:3]
	s_nop 0
	v_pk_add_f32 v[2:3], v[2:3], v[0:1] op_sel_hi:[1,0]
	v_mul_f32_e32 v0, v75, v75
	v_pk_fma_f32 v[2:3], v[74:75], v[74:75], v[2:3]
	s_nop 0
	v_pk_add_f32 v[2:3], v[2:3], v[0:1] op_sel_hi:[1,0]
	s_nop 0
	v_mov_b32_e32 v0, v2
	s_nop 1
	v_permlane32_swap_b32_e32 v2, v0
	v_add_f32_e32 v0, v2, v0
	v_fmamk_f32 v0, v0, 0x3c000000, v220
	v_cmp_gt_f32_e32 vcc, s65, v0
	v_mul_f32_e32 v2, 0x4b800000, v0
	s_nop 0
	v_cndmask_b32_e32 v0, v0, v2, vcc
	v_rsq_f32_e32 v0, v0
	s_nop 0
	v_mul_f32_e32 v2, 0x45800000, v0
	v_cndmask_b32_e32 v0, v0, v2, vcc
	v_mul_f32_e32 v0, v152, v0
	v_pk_mul_f32 v[2:3], v[64:65], v[0:1] op_sel_hi:[1,0]
	s_nop 0
	v_cvt_pk_bf16_f32 v74, v2, v3
	v_pk_mul_f32 v[2:3], v[14:15], v[0:1] op_sel_hi:[1,0]
	s_nop 0
	v_cvt_pk_bf16_f32 v75, v2, v3
	v_pk_mul_f32 v[2:3], v[12:13], v[0:1] op_sel_hi:[1,0]
	s_nop 0
	v_cvt_pk_bf16_f32 v76, v2, v3
	v_pk_mul_f32 v[2:3], v[10:11], v[0:1] op_sel_hi:[1,0]
	s_nop 0
	v_permlane32_swap_b32_e32 v74, v76
	v_cvt_pk_bf16_f32 v77, v2, v3
	v_add_co_u32_e32 v2, vcc, s56, v8
	s_nop 0
	v_permlane32_swap_b32_e32 v75, v77
	v_addc_co_u32_e32 v3, vcc, 0, v9, vcc
	global_store_dwordx4 v[2:3], v[74:77], off offset:3072
	v_pk_mul_f32 v[2:3], v[0:1], v[72:73] op_sel_hi:[0,1]
	v_cvt_pk_bf16_f32 v6, v2, v3
	v_pk_mul_f32 v[2:3], v[0:1], v[70:71] op_sel_hi:[0,1]
	v_cvt_pk_bf16_f32 v7, v2, v3
	v_pk_mul_f32 v[2:3], v[0:1], v[68:69] op_sel_hi:[0,1]
	v_cvt_pk_bf16_f32 v8, v2, v3
	v_pk_mul_f32 v[2:3], v[0:1], v[66:67] op_sel_hi:[0,1]
	v_cvt_pk_bf16_f32 v9, v2, v3
	v_permlane32_swap_b32_e32 v6, v8
	s_nop 0
	v_permlane32_swap_b32_e32 v7, v9
	v_pk_mul_f32 v[2:3], v[0:1], v[48:49] op_sel_hi:[0,1]
	global_store_dwordx4 v[4:5], v[6:9], off offset:32
	s_nop 1
	v_cvt_pk_bf16_f32 v6, v2, v3
	v_pk_mul_f32 v[2:3], v[0:1], v[50:51] op_sel_hi:[0,1]
	v_cvt_pk_bf16_f32 v7, v2, v3
	v_pk_mul_f32 v[2:3], v[0:1], v[52:53] op_sel_hi:[0,1]
	v_cvt_pk_bf16_f32 v8, v2, v3
	v_pk_mul_f32 v[2:3], v[0:1], v[54:55] op_sel_hi:[0,1]
	v_cvt_pk_bf16_f32 v9, v2, v3
	v_permlane32_swap_b32_e32 v6, v8
	s_nop 0
	v_permlane32_swap_b32_e32 v7, v9
	v_pk_mul_f32 v[2:3], v[0:1], v[56:57] op_sel_hi:[0,1]
	global_store_dwordx4 v[4:5], v[6:9], off offset:64
	s_nop 1
	v_cvt_pk_bf16_f32 v6, v2, v3
	v_pk_mul_f32 v[2:3], v[0:1], v[58:59] op_sel_hi:[0,1]
	v_cvt_pk_bf16_f32 v7, v2, v3
	v_pk_mul_f32 v[2:3], v[0:1], v[60:61] op_sel_hi:[0,1]
	v_cvt_pk_bf16_f32 v8, v2, v3
	v_pk_mul_f32 v[2:3], v[0:1], v[62:63] op_sel_hi:[0,1]
	v_cvt_pk_bf16_f32 v9, v2, v3
	v_permlane32_swap_b32_e32 v6, v8
	s_nop 0
	v_permlane32_swap_b32_e32 v7, v9
	v_pk_mul_f32 v[2:3], v[0:1], v[32:33] op_sel_hi:[0,1]
	global_store_dwordx4 v[4:5], v[6:9], off offset:96
	s_nop 1
	v_cvt_pk_bf16_f32 v6, v2, v3
	v_pk_mul_f32 v[2:3], v[0:1], v[34:35] op_sel_hi:[0,1]
	v_cvt_pk_bf16_f32 v7, v2, v3
	v_pk_mul_f32 v[2:3], v[0:1], v[36:37] op_sel_hi:[0,1]
	v_cvt_pk_bf16_f32 v8, v2, v3
	v_pk_mul_f32 v[2:3], v[0:1], v[38:39] op_sel_hi:[0,1]
	v_cvt_pk_bf16_f32 v9, v2, v3
	v_permlane32_swap_b32_e32 v6, v8
	s_nop 0
	v_permlane32_swap_b32_e32 v7, v9
	v_pk_mul_f32 v[2:3], v[0:1], v[40:41] op_sel_hi:[0,1]
	global_store_dwordx4 v[4:5], v[6:9], off offset:128
	s_nop 1
	v_cvt_pk_bf16_f32 v6, v2, v3
	v_pk_mul_f32 v[2:3], v[0:1], v[42:43] op_sel_hi:[0,1]
	v_cvt_pk_bf16_f32 v7, v2, v3
	v_pk_mul_f32 v[2:3], v[0:1], v[44:45] op_sel_hi:[0,1]
	v_cvt_pk_bf16_f32 v8, v2, v3
	v_pk_mul_f32 v[2:3], v[0:1], v[46:47] op_sel_hi:[0,1]
	v_cvt_pk_bf16_f32 v9, v2, v3
	v_permlane32_swap_b32_e32 v6, v8
	s_nop 0
	v_permlane32_swap_b32_e32 v7, v9
	v_pk_mul_f32 v[2:3], v[0:1], v[16:17] op_sel_hi:[0,1]
	global_store_dwordx4 v[4:5], v[6:9], off offset:160
	s_nop 1
	v_cvt_pk_bf16_f32 v6, v2, v3
	v_pk_mul_f32 v[2:3], v[0:1], v[18:19] op_sel_hi:[0,1]
	v_cvt_pk_bf16_f32 v7, v2, v3
	v_pk_mul_f32 v[2:3], v[0:1], v[20:21] op_sel_hi:[0,1]
	v_cvt_pk_bf16_f32 v8, v2, v3
	v_pk_mul_f32 v[2:3], v[0:1], v[22:23] op_sel_hi:[0,1]
	v_cvt_pk_bf16_f32 v9, v2, v3
	v_permlane32_swap_b32_e32 v6, v8
	s_nop 0
	v_permlane32_swap_b32_e32 v7, v9
	v_pk_mul_f32 v[2:3], v[0:1], v[24:25] op_sel_hi:[0,1]
	global_store_dwordx4 v[4:5], v[6:9], off offset:192
	s_nop 1
	v_cvt_pk_bf16_f32 v6, v2, v3
	v_pk_mul_f32 v[2:3], v[0:1], v[26:27] op_sel_hi:[0,1]
	v_cvt_pk_bf16_f32 v7, v2, v3
	v_pk_mul_f32 v[2:3], v[0:1], v[28:29] op_sel_hi:[0,1]
	v_cvt_pk_bf16_f32 v8, v2, v3
	v_pk_mul_f32 v[2:3], v[0:1], v[30:31] op_sel_hi:[0,1]
	v_cvt_pk_bf16_f32 v9, v2, v3
	v_permlane32_swap_b32_e32 v6, v8
	s_nop 0
	v_permlane32_swap_b32_e32 v7, v9
	global_store_dwordx4 v[4:5], v[6:9], off offset:224
